# baseline (speedup 1.0000x reference)
.LBB0_6:
	s_or_b64 exec, exec, s[4:5]
	s_waitcnt vmcnt(14)
	v_mul_f32_e32 v67, v63, v63
	v_fmac_f32_e32 v67, v62, v62
	v_fmac_f32_e32 v67, v64, v64
	v_fmac_f32_e32 v67, v65, v65
	v_fmac_f32_e32 v67, v58, v58
	v_fmac_f32_e32 v67, v59, v59
	v_fmac_f32_e32 v67, v60, v60
	v_fmac_f32_e32 v67, v61, v61
	v_add_f32_e32 v75, v62, v63
	v_add_f32_e32 v83, v64, v65
	v_add_f32_e32 v75, v75, v83
	v_add_f32_e32 v84, v58, v59
	v_add_f32_e32 v85, v60, v61
	v_add_f32_e32 v84, v84, v85
	v_add_f32_e32 v75, v75, v84
	s_waitcnt vmcnt(12)
	v_mul_f32_e32 v68, v51, v51
	v_fmac_f32_e32 v68, v50, v50
	v_fmac_f32_e32 v68, v52, v52
	v_fmac_f32_e32 v68, v53, v53
	v_fmac_f32_e32 v68, v46, v46
	v_fmac_f32_e32 v68, v47, v47
	v_fmac_f32_e32 v68, v48, v48
	v_fmac_f32_e32 v68, v49, v49
	v_add_f32_e32 v76, v50, v51
	v_add_f32_e32 v83, v52, v53
	v_add_f32_e32 v76, v76, v83
	v_add_f32_e32 v84, v46, v47
	v_add_f32_e32 v85, v48, v49
	v_add_f32_e32 v84, v84, v85
	v_add_f32_e32 v76, v76, v84
	s_waitcnt vmcnt(8)
	v_mul_f32_e32 v71, v31, v31
	v_fmac_f32_e32 v71, v30, v30
	v_fmac_f32_e32 v71, v32, v32
	v_fmac_f32_e32 v71, v33, v33
	v_fmac_f32_e32 v71, v26, v26
	v_fmac_f32_e32 v71, v27, v27
	v_fmac_f32_e32 v71, v28, v28
	v_fmac_f32_e32 v71, v29, v29
	v_add_f32_e32 v79, v30, v31
	v_add_f32_e32 v83, v32, v33
	v_add_f32_e32 v79, v79, v83
	v_add_f32_e32 v84, v26, v27
	v_add_f32_e32 v85, v28, v29
	v_add_f32_e32 v84, v84, v85
	v_add_f32_e32 v79, v79, v84
	s_waitcnt vmcnt(6)
	v_mul_f32_e32 v72, v23, v23
	v_fmac_f32_e32 v72, v22, v22
	v_fmac_f32_e32 v72, v24, v24
	v_fmac_f32_e32 v72, v25, v25
	v_fmac_f32_e32 v72, v18, v18
	v_fmac_f32_e32 v72, v19, v19
	v_fmac_f32_e32 v72, v20, v20
	v_fmac_f32_e32 v72, v21, v21
	v_add_f32_e32 v80, v22, v23
	v_add_f32_e32 v83, v24, v25
	v_add_f32_e32 v80, v80, v83
	v_add_f32_e32 v84, v18, v19
	v_add_f32_e32 v85, v20, v21
	v_add_f32_e32 v84, v84, v85
	v_add_f32_e32 v80, v80, v84
	s_waitcnt vmcnt(5)
	v_mul_f32_e32 v70, v35, v35
	v_fmac_f32_e32 v70, v34, v34
	v_fmac_f32_e32 v70, v36, v36
	v_fmac_f32_e32 v70, v37, v37
	v_fmac_f32_e32 v70, v38, v38
	v_fmac_f32_e32 v70, v39, v39
	v_fmac_f32_e32 v70, v40, v40
	v_fmac_f32_e32 v70, v41, v41
	v_add_f32_e32 v78, v34, v35
	v_add_f32_e32 v83, v36, v37
	v_add_f32_e32 v78, v78, v83
	v_add_f32_e32 v84, v38, v39
	v_add_f32_e32 v85, v40, v41
	v_add_f32_e32 v84, v84, v85
	v_add_f32_e32 v78, v78, v84
	s_waitcnt vmcnt(3)
	v_mul_f32_e32 v73, v15, v15
	v_fmac_f32_e32 v73, v14, v14
	v_fmac_f32_e32 v73, v16, v16
	v_fmac_f32_e32 v73, v17, v17
	v_fmac_f32_e32 v73, v10, v10
	v_fmac_f32_e32 v73, v11, v11
	v_fmac_f32_e32 v73, v12, v12
	v_fmac_f32_e32 v73, v13, v13
	v_add_f32_e32 v81, v14, v15
	v_add_f32_e32 v83, v16, v17
	v_add_f32_e32 v81, v81, v83
	v_add_f32_e32 v84, v10, v11
	v_add_f32_e32 v85, v12, v13
	v_add_f32_e32 v84, v84, v85
	v_add_f32_e32 v81, v81, v84
	s_waitcnt vmcnt(1)
	v_mul_f32_e32 v69, v55, v55
	v_fmac_f32_e32 v69, v54, v54
	v_fmac_f32_e32 v69, v56, v56
	v_fmac_f32_e32 v69, v57, v57
	v_fmac_f32_e32 v69, v42, v42
	v_fmac_f32_e32 v69, v43, v43
	v_fmac_f32_e32 v69, v44, v44
	v_fmac_f32_e32 v69, v45, v45
	v_add_f32_e32 v77, v54, v55
	v_add_f32_e32 v83, v56, v57
	v_add_f32_e32 v77, v77, v83
	v_add_f32_e32 v84, v42, v43
	v_add_f32_e32 v85, v44, v45
	v_add_f32_e32 v84, v84, v85
	v_add_f32_e32 v77, v77, v84
	s_waitcnt vmcnt(0)
	v_mul_f32_e32 v74, v7, v7
	v_fmac_f32_e32 v74, v6, v6
	v_fmac_f32_e32 v74, v8, v8
	v_fmac_f32_e32 v74, v9, v9
	v_fmac_f32_e32 v74, v2, v2
	v_fmac_f32_e32 v74, v3, v3
	v_fmac_f32_e32 v74, v4, v4
	v_fmac_f32_e32 v74, v5, v5
	v_add_f32_e32 v82, v6, v7
	v_add_f32_e32 v83, v8, v9
	v_add_f32_e32 v82, v82, v83
	v_add_f32_e32 v84, v2, v3
	v_add_f32_e32 v85, v4, v5
	v_add_f32_e32 v84, v84, v85
	v_add_f32_e32 v82, v82, v84
	v_and_b32_e32 v83, 8, v0
	v_cmp_ne_u32_e64 s[6:7], 0, v83
	v_permlane32_swap_b32_e32 v67, v71
	v_permlane32_swap_b32_e32 v75, v79
	v_permlane32_swap_b32_e32 v68, v72
	v_permlane32_swap_b32_e32 v76, v80
	v_permlane32_swap_b32_e32 v69, v73
	v_permlane32_swap_b32_e32 v77, v81
	v_permlane32_swap_b32_e32 v70, v74
	v_permlane32_swap_b32_e32 v78, v82
	v_add_f32_e32 v67, v67, v71
	v_add_f32_e32 v75, v75, v79
	v_add_f32_e32 v68, v68, v72
	v_add_f32_e32 v76, v76, v80
	v_add_f32_e32 v69, v69, v73
	v_add_f32_e32 v77, v77, v81
	v_add_f32_e32 v70, v70, v74
	v_add_f32_e32 v78, v78, v82
	s_nop 1
	v_permlane16_swap_b32_e32 v67, v69
	v_permlane16_swap_b32_e32 v75, v77
	v_permlane16_swap_b32_e32 v68, v70
	v_permlane16_swap_b32_e32 v76, v78
	v_add_f32_e32 v67, v67, v69
	v_add_f32_e32 v75, v75, v77
	v_add_f32_e32 v68, v68, v70
	v_add_f32_e32 v76, v76, v78
	v_cndmask_b32_e64 v83, v67, v68, s[6:7]
	v_cndmask_b32_e64 v84, v68, v67, s[6:7]
	v_cndmask_b32_e64 v85, v75, v76, s[6:7]
	v_cndmask_b32_e64 v86, v76, v75, s[6:7]
	s_nop 1
	v_add_f32_dpp v67, v84, v83 row_ror:8 row_mask:0xf bank_mask:0xf
	v_add_f32_dpp v69, v86, v85 row_ror:8 row_mask:0xf bank_mask:0xf
	s_nop 1
	v_add_f32_dpp v67, v67, v67 row_half_mirror row_mask:0xf bank_mask:0xf
	v_add_f32_dpp v69, v69, v69 row_half_mirror row_mask:0xf bank_mask:0xf
	s_nop 1
	v_add_f32_dpp v67, v67, v67 quad_perm:[2,3,0,1] row_mask:0xf bank_mask:0xf
	v_add_f32_dpp v69, v69, v69 quad_perm:[2,3,0,1] row_mask:0xf bank_mask:0xf
	s_nop 1
	v_add_f32_dpp v67, v67, v67 quad_perm:[1,0,3,2] row_mask:0xf bank_mask:0xf
	v_add_f32_dpp v69, v69, v69 quad_perm:[1,0,3,2] row_mask:0xf bank_mask:0xf
	s_mov_b32 s3, 0xf800000
	v_mul_f32_e32 v70, 0x4f800000, v67
	v_cmp_gt_f32_e32 vcc, s3, v67
	s_nop 1
	v_cndmask_b32_e32 v67, v67, v70, vcc
	v_sqrt_f32_e32 v70, v67
	s_nop 0
	v_add_u32_e32 v68, -1, v70
	v_fma_f32 v73, -v68, v70, v67
	v_cmp_ge_f32_e64 s[4:5], 0, v73
	v_add_u32_e32 v73, 1, v70
	s_nop 0
	v_cndmask_b32_e64 v68, v70, v68, s[4:5]
	v_fma_f32 v70, -v73, v70, v67
	v_cmp_lt_f32_e64 s[4:5], 0, v70
	s_nop 1
	v_cndmask_b32_e64 v68, v68, v73, s[4:5]
	v_mul_f32_e32 v70, 0x37800000, v68
	v_cndmask_b32_e32 v68, v68, v70, vcc
	v_mov_b32_e32 v70, 0x260
	v_cmp_class_f32_e32 vcc, v67, v70
	s_nop 1
	v_cndmask_b32_e32 v67, v68, v67, vcc
	v_max_f32_e32 v68, 0x322bcc77, v67
	v_div_scale_f32 v67, s[4:5], v68, v68, 1.0
	v_rcp_f32_e32 v73, v67
	s_load_dwordx2 s[4:5], s[0:1], 0x8
	v_fma_f32 v71, -v67, v73, 1.0
	v_fmac_f32_e32 v73, v71, v73
	v_div_scale_f32 v71, vcc, 1.0, v68, 1.0
	v_mul_f32_e32 v72, v71, v73
	v_fma_f32 v74, -v67, v72, v71
	v_fmac_f32_e32 v72, v74, v73
	v_fma_f32 v67, -v67, v72, v71
	v_div_fmas_f32 v71, v67, v73, v72
	v_mov_b32_e32 v70, 0
	v_and_b32_e32 v67, 7, v0
	v_cmp_ne_u32_e32 vcc, 0, v67
	v_lshlrev_b32_e32 v67, 3, v66
	s_and_saveexec_b64 s[6:7], vcc
	s_xor_b64 s[6:7], exec, s[6:7]
	v_lshlrev_b32_e32 v67, 3, v66
	s_or_saveexec_b64 s[6:7], s[6:7]
	v_div_fixup_f32 v66, v71, v68, 1.0
	s_xor_b64 exec, exec, s[6:7]
	s_cbranch_execz .LBB0_10
	s_load_dwordx2 s[0:1], s[0:1], 0x10
	s_waitcnt lgkmcnt(0)
	v_add_f32_e32 v68, v69, v70
	v_mul_f32_e32 v70, v68, v66
	s_lshl_b32 s3, s2, 5
	v_lshrrev_b32_e32 v68, 3, v1
	v_or3_b32 v68, v67, s3, v68
	v_ashrrev_i32_e32 v69, 31, v68
	v_lshl_add_u64 v[68:69], v[68:69], 2, s[0:1]
	global_store_dword v[68:69], v70, off
